# shortpro
# baseline (speedup 1.0000x reference)
_Z11prep_kernelPKfS0_PKiS2_S0_S0_S0_S0_S0_S0_Pc:
	s_load_dwordx4 s[28:31], s[0:1], 0x40
	s_load_dwordx8 s[12:19], s[0:1], 0x0
	s_load_dwordx8 s[20:27], s[0:1], 0x20
	s_load_dwordx2 s[32:33], s[0:1], 0x50
	s_load_dword s40, s[0:1], 0x80
	s_getpc_b64 s[36:37]
	s_add_u32 s36, s36, _Z11attn_kernelILi4EEvPKfS1_S1_S1_S1_S1_PKcPf@rel32@lo+4
	s_addc_u32 s37, s37, _Z11attn_kernelILi4EEvPKfS1_S1_S1_S1_S1_PKcPf@rel32@hi+12
	v_and_b32_e32 v192, 63, v0
	v_lshlrev_b32_e32 v192, 7, v192
	v_min_u32_e32 v192, 0x1180, v192
	global_load_dword v192, v192, s[36:37]
	s_lshr_b32 s4, s2, 2
	v_lshrrev_b32_e32 v2, 6, v0
	s_and_b32 s4, s4, 0x1ffffffe
	v_and_b32_e32 v1, 15, v0
	s_and_b32 s3, s2, 7
	v_or_b32_e32 v2, s4, v2
	v_lshl_or_b32 v88, v2, 3, s3
	v_cmp_gt_u32_e64 s[10:11], 14, v1
	v_mul_lo_u32 v7, v88, 14
	v_and_b32_e32 v105, 63, v0
	v_cndmask_b32_e64 v6, 13, v1, s[10:11]
	v_add_u32_e32 v2, v7, v6
	v_mul_u32_u24_e32 v4, 12, v2
	v_lshlrev_b32_e32 v5, 2, v6
	v_cmp_gt_u32_e64 s[8:9], 48, v105
	v_cmp_gt_u32_e64 s[6:7], 14, v105
	v_lshlrev_b32_e32 v118, 1, v0
	v_lshrrev_b32_e32 v104, 4, v0
	v_cndmask_b32_e64 v8, 0, v105, s[8:9]
	v_cndmask_b32_e64 v9, 0, v105, s[6:7]
	v_mad_u32_u24 v8, v88, 48, v8
	v_add_lshl_u32 v9, v7, v9, 2
	v_lshlrev_b32_e32 v8, 2, v8
	s_lshl_b32 s2, s2, 3
	s_and_b32 s2, s2, 0x78
	v_and_b32_e32 v106, 30, v118
	v_or_b32_e32 v107, s2, v104
	v_cmp_gt_u32_e64 s[2:3], 23, v106
	v_or_b32_e32 v10, 1, v106
	v_cmp_gt_u32_e64 s[4:5], 23, v10
	v_lshlrev_b32_e32 v11, 7, v106
	v_lshlrev_b32_e32 v10, 7, v10
	v_cndmask_b32_e64 v11, 0, v11, s[2:3]
	v_cndmask_b32_e64 v10, 0, v10, s[4:5]
	v_or_b32_e32 v11, v11, v107
	v_or_b32_e32 v10, v10, v107
	v_lshlrev_b32_e32 v11, 2, v11
	v_lshlrev_b32_e32 v10, 2, v10
	v_lshlrev_b32_e32 v12, 2, v107
	v_lshlrev_b32_e32 v119, 5, v0
	v_lshlrev_b32_e32 v13, 2, v0
	v_and_b32_e32 v109, 12, v13
	v_and_b32_e32 v91, 0xf80, v119
	v_lshl_or_b32 v91, v109, 2, v91
	v_or_b32_e32 v92, 0x1000, v91
	v_lshlrev_b32_e32 v90, 9, v2
	v_and_b32_e32 v16, 48, v0
	v_or_b32_e32 v90, v90, v16
	v_or_b32_e32 v112, 0x80, v0
	v_or_b32_e32 v111, 0x180, v0
	v_or_b32_e32 v108, 0x280, v0
	v_mov_b32_e32 v87, 0
	v_bfe_u32 v110, v0, 4, 2
	s_waitcnt lgkmcnt(0)
	global_load_dwordx3 v[82:84], v4, s[12:13]
	global_load_dword v85, v5, s[26:27]
	global_load_dword v114, v8, s[18:19]
	global_load_dword v115, v9, s[16:17]
	global_load_dword v116, v11, s[28:29]
	global_load_dword v113, v10, s[28:29]
	global_load_dword v117, v12, s[30:31]
	global_load_dwordx4 v[66:69], v91, s[20:21]
	global_load_dwordx4 v[70:73], v91, s[20:21] offset:64
	global_load_dwordx4 v[74:77], v92, s[20:21]
	global_load_dwordx4 v[78:81], v92, s[20:21] offset:64
	global_load_dwordx4 v[58:61], v91, s[22:23]
	global_load_dwordx4 v[62:65], v91, s[22:23] offset:64
	global_load_dwordx4 v[50:53], v92, s[22:23]
	global_load_dwordx4 v[54:57], v92, s[22:23] offset:64
	global_load_dwordx4 v[42:45], v91, s[24:25]
	global_load_dwordx4 v[46:49], v91, s[24:25] offset:64
	global_load_dwordx4 v[34:37], v92, s[24:25]
	global_load_dwordx4 v[38:41], v92, s[24:25] offset:64
	global_load_dwordx4 v[26:29], v90, s[14:15] nt
	global_load_dwordx4 v[30:33], v90, s[14:15] offset:64 nt
	global_load_dwordx4 v[18:21], v90, s[14:15] offset:128 nt
	global_load_dwordx4 v[22:25], v90, s[14:15] offset:192 nt
	global_load_dwordx4 v[10:13], v90, s[14:15] offset:256 nt
	global_load_dwordx4 v[14:17], v90, s[14:15] offset:320 nt
	global_load_dwordx4 v[2:5], v90, s[14:15] offset:384 nt
	global_load_dwordx4 v[6:9], v90, s[14:15] offset:448 nt
	s_movk_i32 s34, 0x60
	v_lshrrev_b32_e32 v136, 1, v0
	v_lshrrev_b32_e32 v193, 3, v0
	v_and_b32_e32 v193, 4, v193
	v_and_b32_e32 v194, 24, v0
	v_and_b32_e32 v195, 2, v136
	v_or3_b32 v193, v193, v194, v195
	v_and_or_b32 v136, v136, s34, v193
	v_mul_u32_u24_e32 v193, 0x110, v109
	v_lshl_add_u32 v136, v136, 1, v193
	v_add_u32_e32 v137, 0x1100, v136
	v_add_u32_e32 v138, 0x2200, v136
	v_lshlrev_b32_e32 v193, 9, v88
	v_and_b32_e32 v194, 0x100, v119
	v_lshlrev_b32_e32 v195, 4, v0
	v_and_b32_e32 v195, 48, v195
	v_or3_b32 v139, v193, v194, v195
	v_and_b32_e32 v194, 8, v118
	v_and_b32_e32 v195, 64, v118
	v_or3_b32 v139, v139, v194, v195
	v_lshlrev_b32_e32 v194, 2, v110
	v_and_b32_e32 v195, 4, v194
	v_or_b32_e32 v139, v139, v195
	v_lshl_or_b32 v140, v1, 5, v193
	v_or_b32_e32 v140, v140, v194
	v_add_u32_e32 v140, 0x80000, v140
	v_lshl_or_b32 v141, v88, 4, v1
	v_lshlrev_b32_e32 v141, 3, v141
	v_add_u32_e32 v141, 0x140000, v141
	v_lshlrev_b32_e32 v195, 8, v88
	v_mul_u32_u24_e32 v196, 43, v105
	v_lshrrev_b32_e32 v196, 9, v196
	v_mul_u32_u24_e32 v196, 12, v196
	v_sub_u32_e32 v197, v105, v196
	v_and_b32_e32 v142, 3, v197
	v_lshrrev_b32_e32 v197, 2, v197
	v_mad_u32_u24 v142, v142, 3, v197
	v_add_u32_e32 v142, v142, v196
	v_lshl_add_u32 v142, v142, 2, v195
	v_add_u32_e32 v142, 0x164000, v142
	v_lshl_add_u32 v143, v105, 2, v195
	v_add_u32_e32 v143, 0x164000, v143
	v_lshlrev_b32_e32 v123, 6, v107
	v_lshl_add_u32 v123, v106, 1, v123
	v_add_u32_e32 v123, 0x160000, v123
	v_lshl_add_u32 v122, v1, 4, v195
	v_or_b32_e32 v122, v122, v194
	v_add_u32_e32 v122, 0x100000, v122
	s_waitcnt vmcnt(26)
	v_mov_b32_e32 v90, v83
	v_mov_b32_e32 v91, v84
	v_lshlrev_b32_e32 v86, 2, v110
	s_waitcnt vmcnt(25)
	v_mul_f32_e32 v84, 0x3fb8aa3b, v85
	s_mov_b32 s14, 0x41700000
	v_exp_f32_e32 v84, v84
	v_cndmask_b32_e64 v94, 0, 1.0, s[10:11]
	v_add_f32_e32 v84, 1.0, v84
	v_cmp_lt_f32_e32 vcc, s14, v85
	v_log_f32_e32 v84, v84
	v_cmp_lt_u32_e64 s[12:13], 15, v105
	v_mul_f32_e32 v84, 0x3f317218, v84
	v_cndmask_b32_e32 v84, v84, v85, vcc
	v_mul_f32_e32 v84, 0xbe715bef, v84
	v_mul_f32_e32 v84, 0x3f3504f3, v84
	v_mul_f32_e32 v84, 0x41800000, v84
	v_cndmask_b32_e64 v99, 0, v84, s[10:11]
	v_mul_f32_e32 v101, -2.0, v99
	v_mul_f32_e32 v100, v82, v82
	v_cmp_gt_u32_e32 vcc, 16, v105
	v_fmac_f32_e32 v100, v90, v90
	v_cmp_eq_u32_e64 s[12:13], 0, v110
	v_fmac_f32_e32 v100, v91, v91
	v_cmp_eq_u32_e64 s[14:15], 1, v110
	v_mul_f32_e32 v83, v101, v82
	v_cmp_eq_u32_e64 s[16:17], 2, v110
	v_mul_f32_e32 v84, v101, v90
	v_mul_f32_e32 v85, v101, v91
	v_mul_f32_e32 v89, v99, v100
	v_mul_f32_e32 v92, v82, v94
	v_mul_f32_e32 v93, v90, v94
	v_mul_f32_e32 v95, v91, v94
	v_mul_f32_e32 v96, v100, v94
	v_cvt_pk_fp8_f32 v88, v83, v83
	v_cvt_pk_fp8_f32 v104, v84, v84
	v_cvt_f32_fp8_e32 v97, v88
	v_cvt_f32_fp8_e32 v98, v104
	v_sub_f32_e32 v97, v83, v97
	v_sub_f32_e32 v98, v84, v98
	v_cvt_pk_fp8_f32 v88, v85, v85
	v_cvt_pk_fp8_f32 v104, v99, v99
	v_cvt_f32_fp8_e32 v101, v88
	v_cvt_f32_fp8_e32 v102, v104
	v_sub_f32_e32 v101, v85, v101
	v_sub_f32_e32 v102, v99, v102
	v_cvt_pk_fp8_f32 v88, v89, v89
	v_cvt_pk_fp8_f32 v104, v92, v92
	v_cvt_f32_fp8_e32 v103, v88
	v_cvt_f32_fp8_e32 v120, v104
	v_sub_f32_e32 v103, v89, v103
	v_sub_f32_e32 v120, v92, v120
	v_cvt_pk_fp8_f32 v88, v93, v93
	v_cvt_pk_fp8_f32 v104, v95, v95
	v_cvt_f32_fp8_e32 v121, v88
	v_cvt_f32_fp8_e32 v86, v104
	v_sub_f32_e32 v121, v93, v121
	v_sub_f32_e32 v86, v95, v86
	v_cvt_pk_fp8_f32 v88, v96, v96
	s_nop 0
	v_cvt_f32_fp8_e32 v87, v88
	s_nop 0
	v_sub_f32_e32 v87, v96, v87
	v_cndmask_b32_e64 v124, v89, v85, s[16:17]
	v_cndmask_b32_e64 v124, v124, v98, s[14:15]
	v_cndmask_b32_e64 v124, v124, v83, s[12:13]
	v_cndmask_b32_e64 v125, v103, v99, s[16:17]
	v_cndmask_b32_e64 v125, v125, v84, s[14:15]
	v_cndmask_b32_e64 v125, v125, v97, s[12:13]
	v_cndmask_b32_e64 v126, 0, v102, s[16:17]
	v_cndmask_b32_e64 v126, v126, v85, s[14:15]
	v_cndmask_b32_e64 v126, v126, v83, s[12:13]
	v_cndmask_b32_e64 v127, 0, v99, s[16:17]
	v_cndmask_b32_e64 v127, v127, v101, s[14:15]
	v_cndmask_b32_e64 v127, v127, v84, s[12:13]
	v_cndmask_b32_e64 v128, v94, v86, s[16:17]
	v_cndmask_b32_e64 v128, v128, v93, s[14:15]
	v_cndmask_b32_e64 v128, v128, v92, s[12:13]
	v_cndmask_b32_e64 v129, v94, v96, s[16:17]
	v_cndmask_b32_e64 v129, v129, v121, s[14:15]
	v_cndmask_b32_e64 v129, v129, v92, s[12:13]
	v_cndmask_b32_e64 v130, 0, v96, s[16:17]
	v_cndmask_b32_e64 v130, v130, v95, s[14:15]
	v_cndmask_b32_e64 v130, v130, v120, s[12:13]
	v_cndmask_b32_e64 v131, 0, v87, s[16:17]
	v_cndmask_b32_e64 v131, v131, v95, s[14:15]
	v_cndmask_b32_e64 v131, v131, v93, s[12:13]
	v_cvt_pk_fp8_f32 v119, v124, v125
	v_cvt_pk_fp8_f32 v103, v128, v129
	v_cvt_pk_fp8_f32 v119, v126, v127 op_sel:[0,0,1]
	v_cvt_pk_fp8_f32 v103, v130, v131 op_sel:[0,0,1]
	s_nop 0
	global_store_dword v139, v119, s[32:33] offset:128
	global_store_dword v140, v103, s[32:33] offset:16
	s_and_saveexec_b64 s[0:1], vcc
	s_cbranch_execz .LBB0_14
	v_cvt_f16_f32_e32 v83, v82
	v_cvt_pk_f16_f32 v90, v90, v91
	s_nop 0
	v_alignbit_b32 v91, 0, v90, 16
	v_pack_b32_f16 v90, v83, v90
	global_store_dwordx2 v141, v[90:91], s[32:33]
